# P10: next unit's 256 token-list entries brought into LDS by LDS-DMA at the unit head; the gather-offset block reads them with ds_read instead of per-lane global loads inside the last K iteration
# baseline (speedup 1.0000x reference)
.LBB0_923:
	s_ashr_i32 s9, s8, 31
	s_ashr_i32 s39, s38, 31
	s_lshl_b64 s[4:5], s[38:39], 19
	s_lshl_b64 s[10:11], s[8:9], 23
	s_add_u32 s10, s37, s10
	s_addc_u32 s11, s50, s11
	s_add_u32 s10, s10, s4
	s_addc_u32 s11, s11, s5
	s_and_b64 s[4:5], s[6:7], exec
	s_cselect_b32 s4, s11, s45
	s_cselect_b32 s5, s10, s44
	s_lshl_b32 s39, s68, 8
	s_lshl_b64 s[14:15], s[8:9], 16
	s_or_b32 s43, s39, 0x80
	s_lshl_b64 s[12:13], s[8:9], 2
	s_add_u32 s12, s18, s12
	s_addc_u32 s13, s19, s13
	s_add_u32 s14, s41, s14
	s_addc_u32 s15, s51, s15
	s_add_u32 s9, s44, 0x100
	v_mov_b32_e32 v34, 0
	s_addc_u32 s69, s45, 0
	s_mov_b32 s70, -2
	s_mov_b64 s[44:45], s[30:31]
	v_mov_b32_e32 v35, v34
	v_mov_b32_e32 v36, v34
	v_mov_b32_e32 v37, v34
	v_mov_b32_e32 v42, v34
	v_mov_b32_e32 v43, v34
	v_mov_b32_e32 v44, v34
	v_mov_b32_e32 v45, v34
	v_mov_b32_e32 v50, v34
	v_mov_b32_e32 v51, v34
	v_mov_b32_e32 v52, v34
	v_mov_b32_e32 v53, v34
	v_mov_b32_e32 v58, v34
	v_mov_b32_e32 v59, v34
	v_mov_b32_e32 v60, v34
	v_mov_b32_e32 v61, v34
	v_mov_b32_e32 v66, v34
	v_mov_b32_e32 v67, v34
	v_mov_b32_e32 v68, v34
	v_mov_b32_e32 v69, v34
	v_mov_b32_e32 v74, v34
	v_mov_b32_e32 v75, v34
	v_mov_b32_e32 v76, v34
	v_mov_b32_e32 v77, v34
	v_mov_b32_e32 v82, v34
	v_mov_b32_e32 v83, v34
	v_mov_b32_e32 v84, v34
	v_mov_b32_e32 v85, v34
	v_mov_b32_e32 v90, v34
	v_mov_b32_e32 v91, v34
	v_mov_b32_e32 v92, v34
	v_mov_b32_e32 v93, v34
	v_mov_b32_e32 v38, v34
	v_mov_b32_e32 v39, v34
	v_mov_b32_e32 v40, v34
	v_mov_b32_e32 v41, v34
	v_mov_b32_e32 v46, v34
	v_mov_b32_e32 v47, v34
	v_mov_b32_e32 v48, v34
	v_mov_b32_e32 v49, v34
	v_mov_b32_e32 v54, v34
	v_mov_b32_e32 v55, v34
	v_mov_b32_e32 v56, v34
	v_mov_b32_e32 v57, v34
	v_mov_b32_e32 v62, v34
	v_mov_b32_e32 v63, v34
	v_mov_b32_e32 v64, v34
	v_mov_b32_e32 v65, v34
	v_mov_b32_e32 v70, v34
	v_mov_b32_e32 v71, v34
	v_mov_b32_e32 v72, v34
	v_mov_b32_e32 v73, v34
	v_mov_b32_e32 v78, v34
	v_mov_b32_e32 v79, v34
	v_mov_b32_e32 v80, v34
	v_mov_b32_e32 v81, v34
	v_mov_b32_e32 v86, v34
	v_mov_b32_e32 v87, v34
	v_mov_b32_e32 v88, v34
	v_mov_b32_e32 v89, v34
	v_mov_b32_e32 v94, v34
	v_mov_b32_e32 v95, v34
	v_mov_b32_e32 v96, v34
	v_mov_b32_e32 v97, v34
	v_mov_b32_e32 v98, v34
	v_mov_b32_e32 v99, v34
	v_mov_b32_e32 v100, v34
	v_mov_b32_e32 v101, v34
	v_mov_b32_e32 v106, v34
	v_mov_b32_e32 v107, v34
	v_mov_b32_e32 v108, v34
	v_mov_b32_e32 v109, v34
	v_mov_b32_e32 v114, v34
	v_mov_b32_e32 v115, v34
	v_mov_b32_e32 v116, v34
	v_mov_b32_e32 v117, v34
	v_mov_b32_e32 v122, v34
	v_mov_b32_e32 v123, v34
	v_mov_b32_e32 v124, v34
	v_mov_b32_e32 v125, v34
	v_mov_b32_e32 v130, v34
	v_mov_b32_e32 v131, v34
	v_mov_b32_e32 v132, v34
	v_mov_b32_e32 v133, v34
	v_mov_b32_e32 v138, v34
	v_mov_b32_e32 v139, v34
	v_mov_b32_e32 v140, v34
	v_mov_b32_e32 v141, v34
	v_mov_b32_e32 v146, v34
	v_mov_b32_e32 v147, v34
	v_mov_b32_e32 v148, v34
	v_mov_b32_e32 v149, v34
	v_mov_b32_e32 v150, v34
	v_mov_b32_e32 v151, v34
	v_mov_b32_e32 v152, v34
	v_mov_b32_e32 v153, v34
	v_mov_b32_e32 v102, v34
	v_mov_b32_e32 v103, v34
	v_mov_b32_e32 v104, v34
	v_mov_b32_e32 v105, v34
	v_mov_b32_e32 v110, v34
	v_mov_b32_e32 v111, v34
	v_mov_b32_e32 v112, v34
	v_mov_b32_e32 v113, v34
	v_mov_b32_e32 v118, v34
	v_mov_b32_e32 v119, v34
	v_mov_b32_e32 v120, v34
	v_mov_b32_e32 v121, v34
	v_mov_b32_e32 v126, v34
	v_mov_b32_e32 v127, v34
	v_mov_b32_e32 v128, v34
	v_mov_b32_e32 v129, v34
	v_mov_b32_e32 v134, v34
	v_mov_b32_e32 v135, v34
	v_mov_b32_e32 v136, v34
	v_mov_b32_e32 v137, v34
	v_mov_b32_e32 v142, v34
	v_mov_b32_e32 v143, v34
	v_mov_b32_e32 v144, v34
	v_mov_b32_e32 v145, v34
	v_mov_b32_e32 v154, v34
	v_mov_b32_e32 v155, v34
	v_mov_b32_e32 v156, v34
	v_mov_b32_e32 v157, v34
	v_mov_b32_e32 v158, v34
	v_mov_b32_e32 v159, v34
	v_mov_b32_e32 v160, v34
	v_mov_b32_e32 v161, v34
	v_readlane_b32 s46, v255, 30
	s_xor_b32 s46, s46, 1
	s_and_b32 s46, s46, 1
	v_writelane_b32 v255, s46, 30
	s_lshl_b32 s46, s46, 10
	s_add_u32 m0, s46, 0x20000
	s_lshl_b32 s48, s42, 14
	s_lshl_b32 s49, s40, 10
	s_add_u32 s48, s48, s49
	s_add_u32 s48, s20, s48
	s_addc_u32 s49, s21, 0
	v_and_b32_e32 v2, 63, v0
	v_lshlrev_b32_e32 v2, 4, v2
	global_load_lds_dwordx4 v2, s[48:49]
	s_and_b64 vcc, exec, s[6:7]
	s_cbranch_vccz .Lmoe_nolist
	s_lshl_b32 s48, s39, 2
	s_add_u32 s48, s14, s48
	s_addc_u32 s49, s15, 0
	s_mov_b32 m0, 0x20c00
	s_nop 0
	global_load_lds_dwordx4 v2, s[48:49]

.LBB0_924:
	v_mov_b32_e32 v165, v0
	s_sub_u32 s48, s12, s18
	s_add_u32 s48, s48, 0x20800
	v_mov_b32_e32 v166, s48
	ds_read_b32 v166, v166
	v_lshlrev_b32_e32 v167, 4, v165
	v_ashrrev_i32_e32 v170, 31, v165
	v_bfe_i32 v171, v165, 27, 1
	v_lshrrev_b32_e32 v170, 26, v170
	v_lshrrev_b32_e32 v171, 22, v171
	v_add_u32_e32 v172, 0x2000, v167
	v_add_u32_e32 v165, v165, v170
	v_add_u32_e32 v170, v167, v171
	v_ashrrev_i32_e32 v171, 31, v172
	v_and_b32_e32 v170, 0xfffffc00, v170
	v_lshrrev_b32_e32 v171, 22, v171
	v_sub_u32_e32 v167, v167, v170
	v_add_u32_e32 v171, v172, v171
	v_lshrrev_b32_e32 v173, 4, v167
	v_ashrrev_i32_e32 v174, 31, v167
	v_ashrrev_i32_e32 v181, 10, v171
	v_bitop3_b32 v182, v173, v167, 32 bitop3:0x6c
	v_lshrrev_b32_e32 v167, 26, v174
	v_mul_i32_i24_e32 v171, 0x400, v181
	v_add_u32_e32 v167, v182, v167
	v_sub_u32_e32 v171, v172, v171
	v_ashrrev_i32_e32 v183, 6, v167
	v_lshrrev_b32_e32 v167, 4, v171
	v_bitop3_b32 v184, v167, v171, 32 bitop3:0x6c
	v_ashrrev_i32_e32 v171, 31, v184
	v_ashrrev_i32_e32 v165, 6, v165
	v_lshrrev_b32_e32 v171, 26, v171
	v_lshlrev_b32_e32 v170, 3, v165
	v_lshlrev_b32_e32 v173, 3, v181
	v_add_u32_e32 v185, v184, v171
	v_and_b32_e32 v170, -16, v170
	v_and_b32_e32 v172, -16, v173
	v_ashrrev_i32_e32 v171, 6, v185
	v_add_u32_e32 v170, v183, v170
	v_add_u32_e32 v171, v171, v172
	v_add_u32_e32 v167, s39, v170
	v_add_u32_e32 v170, s43, v170
	v_add_u32_e32 v172, s39, v171
	v_add_u32_e32 v171, s43, v171
	v_lshlrev_b32_e32 v165, 5, v165
	v_and_b32_e32 v165, 32, v165
	s_waitcnt lgkmcnt(0)
	v_readfirstlane_b32 s48, v166
	s_add_i32 s48, s48, -1
	s_nop 0
	v_min_i32_e32 v166, s48, v167
	v_min_i32_e32 v170, s48, v170
	v_min_i32_e32 v172, s48, v172
	v_min_i32_e32 v174, s48, v171
	v_ashrrev_i32_e32 v167, 31, v166
	v_ashrrev_i32_e32 v171, 31, v170
	v_ashrrev_i32_e32 v173, 31, v172
	v_ashrrev_i32_e32 v175, 31, v174
	v_subrev_u32_e32 v166, s39, v166
	v_lshlrev_b32_e32 v166, 2, v166
	v_add_u32_e32 v166, 0x20c00, v166
	v_subrev_u32_e32 v170, s39, v170
	v_lshlrev_b32_e32 v170, 2, v170
	v_add_u32_e32 v170, 0x20c00, v170
	v_subrev_u32_e32 v172, s39, v172
	v_lshlrev_b32_e32 v172, 2, v172
	v_add_u32_e32 v172, 0x20c00, v172
	v_subrev_u32_e32 v174, s39, v174
	v_lshlrev_b32_e32 v174, 2, v174
	v_add_u32_e32 v174, 0x20c00, v174
	ds_read_b32 v166, v166
	s_nop 0
	ds_read_b32 v170, v170
	s_nop 0
	ds_read_b32 v171, v172
	s_nop 0
	ds_read_b32 v172, v174
	v_mul_i32_i24_e32 v174, 64, v183
	v_sub_u32_e32 v174, v182, v174
	v_ashrrev_i16_sdwa v174, v1, sext(v174) dst_sel:DWORD dst_unused:UNUSED_PAD src0_sel:DWORD src1_sel:BYTE_0
	v_bfe_i32 v174, v174, 0, 16
	v_add_lshl_u32 v165, v165, v174, 1
	v_and_b32_e32 v174, 0xc0, v185
	v_sub_u32_e32 v174, v184, v174
	v_lshlrev_b32_e32 v173, 5, v181
	v_ashrrev_i16_sdwa v174, v1, sext(v174) dst_sel:DWORD dst_unused:UNUSED_PAD src0_sel:DWORD src1_sel:BYTE_0
	v_and_b32_e32 v173, 32, v173
	v_bfe_i32 v174, v174, 0, 16
	v_add_lshl_u32 v173, v173, v174, 1
	v_mov_b32_e32 v167, v163
	s_waitcnt lgkmcnt(3)
	v_lshlrev_b32_e32 v166, 9, v166
	s_waitcnt lgkmcnt(2)
	v_lshlrev_b32_e32 v170, 9, v170
	s_waitcnt lgkmcnt(1)
	v_lshlrev_b32_e32 v171, 9, v171
	s_waitcnt lgkmcnt(0)
	v_lshlrev_b32_e32 v172, 9, v172
	v_and_b32_e32 v166, 0xfffff800, v166
	v_and_b32_e32 v174, 0xfffff800, v170
	v_and_b32_e32 v171, 0xfffff800, v171
	v_and_b32_e32 v175, 0xfffff800, v172
	v_add_u32_e32 v170, v165, v166
	v_add_u32_e32 v166, v165, v174
	v_add_u32_e32 v172, v173, v171
	v_add_u32_e32 v174, v173, v175
